# v026 + grid barrier: the XCD leader releases its XCD (XGEN add) before its own acquire invalidate instead of after
# baseline (speedup 1.0000x reference)
; __device__ __forceinline__ unsigned xb_add(unsigned* p, unsigned v) { return __hip_atomic_fetch_add(p, v, __ATOMIC_RELAXED, __HIP_MEMORY_SCOPE_AGENT); }
; __device__ __forceinline__ void xcd_barrier(const XcdBarrier& b, int wave_s) {
;     ...
;             __builtin_amdgcn_fence(__ATOMIC_ACQUIRE, "agent");
;             xb_add(&bar[XB_XGEN(bx_)], 1u);
;             asm volatile("s_waitcnt vmcnt(0)" ::: "memory");
.LBB0_82:
	s_or_b64 exec, exec, s[2:3]
	v_mov_b32_e32 v0, s23
	v_add_co_u32_e32 v0, vcc, 0x2000, v0
	v_mov_b32_e32 v1, s22
	s_nop 0
	v_addc_co_u32_e32 v1, vcc, 0, v1, vcc
	s_waitcnt vmcnt(0) lgkmcnt(0)
	flat_atomic_add v[0:1], v203 offset:1024
	buffer_inv sc1
	s_waitcnt vmcnt(0)
